# speedup vs baseline: 1.0126x; 1.0126x over previous
.Lpro_wc_done:
	v_cmp_gt_u32_e32 vcc, 4, v1
	s_nop 1
	s_and_saveexec_b64 s[0:1], vcc
	v_lshl_add_u32 v119, v1, 5, s8
	ds_read_b64 v[120:121], v119
	s_waitcnt lgkmcnt(0)
	v_max_i32_e32 v120, 1, v120
	v_max_i32_e32 v121, 1, v121
	v_cvt_f32_u32_e32 v120, v120
	v_cvt_f32_u32_e32 v121, v121
	v_div_scale_f32 v124, s[38:39], v120, v120, 1.0
	v_rcp_f32_e32 v125, v124
	s_nop 0
	v_fma_f32 v126, -v124, v125, 1.0
	v_fmac_f32_e32 v125, v126, v125
	v_div_scale_f32 v126, vcc, 1.0, v120, 1.0
	v_mul_f32_e32 v127, v126, v125
	v_fma_f32 v118, -v124, v127, v126
	v_fmac_f32_e32 v127, v118, v125
	v_fma_f32 v124, -v124, v127, v126
	s_nop 0
	v_div_fmas_f32 v124, v124, v125, v127
	v_div_fixup_f32 v122, v124, v120, 1.0
	v_div_scale_f32 v124, s[38:39], v121, v121, 1.0
	v_rcp_f32_e32 v125, v124
	s_nop 0
	v_fma_f32 v126, -v124, v125, 1.0
	v_fmac_f32_e32 v125, v126, v125
	v_div_scale_f32 v126, vcc, 1.0, v121, 1.0
	v_mul_f32_e32 v127, v126, v125
	v_fma_f32 v118, -v124, v127, v126
	v_fmac_f32_e32 v127, v118, v125
	v_fma_f32 v124, -v124, v127, v126
	s_nop 0
	v_div_fmas_f32 v124, v124, v125, v127
	v_div_fixup_f32 v123, v124, v121, 1.0
	ds_write_b64 v119, v[122:123] offset:24
	v_readfirstlane_b32 s90, v122
	v_readfirstlane_b32 s91, v123
	s_or_b64 exec, exec, s[0:1]
	s_lshr_b32 s0, s33, 8
	s_lshl_b32 s1, s37, 4
	v_and_or_b32 v104, s1, 48, v82
	s_waitcnt lgkmcnt(0)
	v_mov_b32_e32 v62, 0x15300
	v_lshl_or_b32 v62, v104, 2, v62
	v_lshlrev_b32_e32 v109, 5, v106
	s_barrier
	ds_read_b32 v105, v62
	v_or_b32_e32 v62, 0x15000, v109
	v_or_b32_e32 v84, 0x15100, v109
	ds_read_b128 v[62:65], v62
	ds_read_b128 v[84:87], v84
	s_lshl_b32 s1, s0, 6
	s_add_i32 s2, s1, 0x14c00
	v_lshlrev_b32_e32 v108, 4, v106
	v_or_b32_e32 v88, s2, v108
	s_waitcnt lgkmcnt(0)
	v_fma_f32 v63, v105, v63, v85
	v_lshlrev_b32_e32 v92, 4, v1
	v_max_f32_e32 v101, 0, v63
	v_or_b32_e32 v63, 0x15010, v109
	ds_read_b128 v[88:91], v88 offset:1536
	v_lshl_or_b32 v100, s0, 11, v92
	v_fma_f32 v62, v105, v62, v84
	v_or_b32_e32 v84, 0x15110, v109
	ds_read_b128 v[92:95], v63
	ds_read_b128 v[96:99], v84
	v_fmac_f32_e32 v87, v105, v65
	v_fma_f32 v63, v105, v64, v86
	v_max_f32_e32 v102, 0, v87
	v_max_f32_e32 v62, 0, v62
	s_waitcnt lgkmcnt(0)
	v_fma_f32 v65, v105, v93, v97
	v_fma_f32 v64, v105, v92, v96
	v_max_f32_e32 v92, 0, v65
	v_fma_f32 v65, v105, v94, v98
	v_fmac_f32_e32 v99, v105, v95
	v_max_f32_e32 v65, 0, v65
	v_max_f32_e32 v84, 0, v99
	v_cvt_pk_f16_f32 v65, v65, v84
	ds_read_b128 v[84:87], v100 offset:36864
	v_max_f32_e32 v64, 0, v64
	v_cvt_pk_f16_f32 v64, v64, v92
	v_or_b32_e32 v92, 0x15080, v109
	v_or_b32_e32 v96, 0x15180, v109
	ds_read_b128 v[92:95], v92
	ds_read_b128 v[96:99], v96
	v_max_f32_e32 v63, 0, v63
	v_cvt_pk_f16_f32 v63, v63, v102
	v_cvt_pk_f16_f32 v62, v62, v101
	ds_read_b128 v[100:103], v100 offset:37888
	s_waitcnt lgkmcnt(1)
	v_fma_f32 v94, v105, v94, v98
	v_mfma_f32_16x16x32_f16 v[62:65], v[84:87], v[62:65], v[88:91]
	v_fma_f32 v84, v105, v92, v96
	v_max_f32_e32 v92, 0, v84
	v_fma_f32 v84, v105, v93, v97
	v_max_f32_e32 v93, 0, v84
	v_or_b32_e32 v84, 0x15090, v109
	v_or_b32_e32 v88, 0x15190, v109
	ds_read_b128 v[84:87], v84
	ds_read_b128 v[88:91], v88
	v_fmac_f32_e32 v99, v105, v95
	v_max_f32_e32 v94, 0, v94
	v_max_f32_e32 v95, 0, v99
	s_add_i32 s1, s1, 0xb000
	s_waitcnt lgkmcnt(0)
	v_fma_f32 v84, v105, v84, v88
	v_fma_f32 v85, v105, v85, v89
	v_fma_f32 v86, v105, v86, v90
	v_fmac_f32_e32 v91, v105, v87
	v_max_f32_e32 v84, 0, v84
	v_max_f32_e32 v85, 0, v85
	v_max_f32_e32 v86, 0, v86
	v_max_f32_e32 v87, 0, v91
	v_cvt_pk_f16_f32 v87, v86, v87
	v_cvt_pk_f16_f32 v86, v84, v85
	v_cvt_pk_f16_f32 v85, v94, v95
	v_cvt_pk_f16_f32 v84, v92, v93
	v_cmp_eq_u32_e64 s[12:13], 1, v106
	v_cmp_eq_u32_e64 s[2:3], 0, v1
	v_mfma_f32_16x16x32_f16 v[62:65], v[100:103], v[84:87], v[62:65]
	v_mul_u32_u24_e32 v84, 0x110, v104
	v_add3_u32 v84, s1, v84, v108
	v_or_b32_e32 v112, 4, v106
	v_or_b32_e32 v116, 60, v106
	s_nop 3
	ds_write_b128 v84, v[62:65]
	v_mbcnt_lo_u32_b32 v62, -1, 0
	v_mbcnt_hi_u32_b32 v62, -1, v62
	v_and_or_b32 v62, v62, 64, v82
	v_lshlrev_b32_e32 v108, 2, v62
	v_mov_b32_e32 v62, 0x13c00
	v_lshl_or_b32 v111, v106, 2, v62
	v_mov_b32_e32 v62, 0xf400
	v_lshl_or_b32 v113, v83, 2, v62
	v_and_b32_e32 v62, 8, v0
	v_cmp_eq_u32_e64 s[4:5], 0, v62
	v_and_b32_e32 v62, 4, v0
	v_cmp_eq_u32_e64 s[6:7], 0, v62
	v_and_b32_e32 v62, 2, v0
	v_and_b32_e32 v0, 1, v0
	v_cmp_eq_u32_e64 s[10:11], 0, v0
	v_mov_b32_e32 v0, 0x13400
	v_cmp_eq_u32_e64 s[8:9], 0, v62
	v_lshl_or_b32 v117, v1, 1, v0
	v_mov_b32_e32 v0, s14
	v_mov_b32_e32 v62, s26
	v_cndmask_b32_e64 v0, v0, v62, s[12:13]
	v_mov_b32_e32 v62, s15
	v_mov_b32_e32 v63, s27
	v_cndmask_b32_e64 v62, v62, v63, s[12:13]
	v_mov_b32_e32 v63, s25
	v_cmp_gt_u32_e64 s[14:15], 16, v1
	v_or_b32_e32 v109, 64, v108
	v_or_b32_e32 v110, 0x80, v108
	v_cndmask_b32_e64 v1, v62, v63, s[14:15]
	v_mov_b32_e32 v62, s24
	v_cndmask_b32_e64 v0, v0, v62, s[14:15]
	v_mov_b32_e32 v62, 0
	s_waitcnt lgkmcnt(0)
	s_barrier
	s_branch .LBB0_74
.LBB0_73:
	s_or_b64 exec, exec, s[0:1]
	s_cmp_gt_i32 s25, -1
	s_mov_b32 s35, s27
	s_mov_b32 s36, s26
	s_mov_b32 s34, s24
	s_mov_b32 s90, s92
	s_mov_b32 s91, s93
	s_cbranch_scc0 .LBB0_120

.LBB0_78:
	s_or_b64 exec, exec, s[0:1]
	v_readfirstlane_b32 s0, v63
	s_lshl_b32 s1, s0, 2
	s_and_b32 s1, s1, 60
	s_ashr_i32 s24, s0, 4
	s_add_i32 s24, s24, s1
	s_add_i32 s24, s24, 1
	s_cmp_lt_i32 s0, 48
	s_cselect_b32 s25, s24, -1
	s_mov_b32 s26, s36
	s_mov_b32 s27, s35
	s_cmp_lt_i32 s25, 0
	s_cbranch_scc1 .Lnl_nopf
	s_lshl_b32 s0, s25, 5
	s_add_i32 s1, s0, 0x14400
	v_mov_b32_e32 v64, s1
	ds_read_b128 v[118:121], v64
	ds_read_b32 v122, v64 offset:16
	ds_read_b64 v[126:127], v64 offset:24
	v_add_u32_e32 v65, s0, v111
	ds_read2_b32 v[124:125], v65 offset1:4
	s_lshl_b32 s0, s25, 8
	v_add_u32_e32 v63, s0, v113
	ds_read_b128 v[86:89], v63
	ds_read_b128 v[90:93], v63 offset:16
	ds_read_b128 v[94:97], v63 offset:32
	ds_read_b128 v[98:101], v63 offset:48
.Lnl_nopf:
	s_waitcnt vmcnt(0) lgkmcnt(0)
	v_pk_add_f32 v[102:103], v[6:7], v[10:11]
	v_pk_add_f32 v[104:105], v[8:9], v[12:13]
	s_cmp_lt_i32 s25, 0
	s_cbranch_scc1 .Lnl_nocat
	v_readfirstlane_b32 s27, v118
	v_readfirstlane_b32 s26, v119
	v_readfirstlane_b32 s92, v126
	v_readfirstlane_b32 s93, v127
	v_mov_b64_e32 v[6:7], 0
	v_mov_b64_e32 v[8:9], 0
	v_mov_b64_e32 v[10:11], 0
	v_mov_b64_e32 v[12:13], 0
	v_cmp_gt_i32_e32 vcc, s26, v106
	s_and_saveexec_b64 s[0:1], vcc
	s_cbranch_execz .Lnl_c0
	v_lshl_or_b32 v63, v124, 8, v107
	global_load_dwordx4 v[6:9], v63, s[18:19] sc1

.Lnl_t_done:
	v_mov_b32_e32 v86, v102
	v_mov_b32_e32 v87, v103
	v_mov_b32_e32 v88, v104
	v_mov_b32_e32 v89, v105
	v_permlane16_swap_b32_e32 v102, v86
	v_permlane16_swap_b32_e32 v103, v87
	v_permlane16_swap_b32_e32 v104, v88
	v_permlane16_swap_b32_e32 v105, v89
	v_add_f32_e32 v90, v102, v86
	v_add_f32_e32 v91, v103, v87
	v_add_f32_e32 v94, v104, v88
	v_add_f32_e32 v95, v105, v89
	v_mov_b32_e32 v86, v82
	v_mov_b32_e32 v87, v83
	v_mov_b32_e32 v88, v84
	v_mov_b32_e32 v89, v85
	v_permlane16_swap_b32_e32 v82, v86
	v_permlane16_swap_b32_e32 v83, v87
	v_permlane16_swap_b32_e32 v84, v88
	v_permlane16_swap_b32_e32 v85, v89
	v_add_f32_e32 v98, v82, v86
	v_add_f32_e32 v99, v83, v87
	v_add_f32_e32 v102, v84, v88
	v_add_f32_e32 v103, v85, v89
	v_mov_b32_e32 v92, v90
	v_mov_b32_e32 v93, v91
	v_mov_b32_e32 v96, v94
	v_mov_b32_e32 v97, v95
	v_mov_b32_e32 v100, v98
	v_mov_b32_e32 v101, v99
	v_mov_b32_e32 v104, v102
	v_mov_b32_e32 v105, v103
	v_permlane32_swap_b32_e32 v90, v92
	v_permlane32_swap_b32_e32 v91, v93
	v_permlane32_swap_b32_e32 v94, v96
	v_permlane32_swap_b32_e32 v95, v97
	v_permlane32_swap_b32_e32 v98, v100
	v_permlane32_swap_b32_e32 v99, v101
	v_permlane32_swap_b32_e32 v102, v104
	v_permlane32_swap_b32_e32 v103, v105
	s_mul_i32 s0, s34, 0x110
	v_add_u32_e32 v63, 0xb000, v107
	v_add_u32_e32 v63, s0, v63
	ds_read_b128 v[82:85], v63
	s_branch .LBB0_118

.LBB0_118:
	v_pk_add_f32 v[64:65], v[90:91], v[92:93]
	s_waitcnt lgkmcnt(0)
	v_pk_add_f32 v[86:87], v[94:95], v[96:97]
	v_pk_add_f32 v[88:89], v[98:99], v[100:101]
	v_pk_add_f32 v[90:91], v[102:103], v[104:105]
	v_mul_f32_e32 v99, v83, v126
	v_mul_f32_e32 v102, v83, v122
	v_fmac_f32_e32 v99, v82, v124
	v_fmac_f32_e32 v102, v82, v120
	v_fmac_f32_e32 v99, v84, v125
	v_fmac_f32_e32 v102, v84, v121
	v_fmac_f32_e32 v99, v85, v123
	v_mov_b32_e32 v92, s91
	v_mov_b32_e32 v94, s90
	v_pk_mul_f32 v[64:65], v[92:93], v[64:65] op_sel_hi:[0,1]
	v_pk_mul_f32 v[88:89], v[94:95], v[88:89] op_sel_hi:[0,1]
	v_pk_mul_f32 v[86:87], v[92:93], v[86:87] op_sel_hi:[0,1]
	v_mul_f32_e32 v93, v65, v115
	v_mul_f32_e32 v97, v65, v126
	v_mul_f32_e32 v100, v65, v122
	v_mul_f32_e32 v103, v65, v89
	v_mul_f32_e32 v65, v83, v65
	v_mul_f32_e32 v63, v115, v126
	v_fmac_f32_e32 v93, v64, v118
	v_fmac_f32_e32 v97, v64, v124
	v_fmac_f32_e32 v100, v64, v120
	v_fmac_f32_e32 v103, v64, v88
	v_fmac_f32_e32 v65, v82, v64
	v_mul_f32_e32 v64, v83, v89
	v_pk_mul_f32 v[90:91], v[94:95], v[90:91] op_sel_hi:[0,1]
	v_fmac_f32_e32 v63, v118, v124
	v_mul_f32_e32 v92, v115, v122
	v_mul_f32_e32 v94, v89, v115
	v_mul_f32_e32 v95, v83, v115
	v_mul_f32_e32 v96, v126, v122
	v_mul_f32_e32 v98, v89, v126
	v_mul_f32_e32 v101, v89, v122
	v_fmac_f32_e32 v64, v82, v88
	v_fmac_f32_e32 v63, v114, v125
	v_fmac_f32_e32 v92, v118, v120
	v_fmac_f32_e32 v94, v88, v118
	v_fmac_f32_e32 v95, v82, v118
	v_fmac_f32_e32 v96, v124, v120
	v_fmac_f32_e32 v98, v88, v124
	v_fmac_f32_e32 v101, v88, v120
	v_fmac_f32_e32 v65, v84, v86
	v_fmac_f32_e32 v64, v84, v90
	v_fmac_f32_e32 v63, v127, v123
	v_fmac_f32_e32 v92, v114, v121
	v_fmac_f32_e32 v93, v86, v114
	v_fmac_f32_e32 v94, v90, v114
	v_fmac_f32_e32 v95, v84, v114
	v_fmac_f32_e32 v96, v125, v121
	v_fmac_f32_e32 v97, v86, v125
	v_fmac_f32_e32 v98, v90, v125
	v_fmac_f32_e32 v100, v86, v121
	v_fmac_f32_e32 v101, v90, v121
	v_fmac_f32_e32 v103, v86, v90
	v_fmac_f32_e32 v65, v85, v87
	v_fmac_f32_e32 v64, v85, v91
	v_fmac_f32_e32 v92, v127, v119
	v_fmac_f32_e32 v93, v87, v127
	v_fmac_f32_e32 v94, v91, v127
	v_fmac_f32_e32 v95, v85, v127
	v_fmac_f32_e32 v96, v123, v119
	v_fmac_f32_e32 v97, v87, v123
	v_fmac_f32_e32 v98, v91, v123
	v_fmac_f32_e32 v100, v87, v119
	v_fmac_f32_e32 v101, v91, v119
	v_fmac_f32_e32 v102, v85, v119
	v_fmac_f32_e32 v103, v87, v91
	v_cndmask_b32_e64 v82, v63, v99, s[4:5]
	v_cndmask_b32_e64 v63, v99, v63, s[4:5]
	v_cndmask_b32_e64 v83, v100, v92, s[4:5]
	v_cndmask_b32_e64 v84, v101, v93, s[4:5]
	v_add_f32_dpp v63, v82, v63 row_ror:8 row_mask:0xf bank_mask:0xf bound_ctrl:1
	v_cndmask_b32_e64 v82, v92, v100, s[4:5]
	v_cndmask_b32_e64 v85, v102, v94, s[4:5]
	v_cndmask_b32_e64 v86, v103, v95, s[4:5]
	v_add_f32_dpp v82, v82, v83 row_ror:8 row_mask:0xf bank_mask:0xf bound_ctrl:1
	v_cndmask_b32_e64 v83, v93, v101, s[4:5]
	v_cndmask_b32_e64 v87, 0, v98, s[4:5]
	s_nop 0
	v_add_f32_dpp v83, v83, v84 row_ror:8 row_mask:0xf bank_mask:0xf bound_ctrl:1
	v_cndmask_b32_e64 v84, v94, v102, s[4:5]
	s_nop 1
	v_add_f32_dpp v84, v84, v85 row_ror:8 row_mask:0xf bank_mask:0xf bound_ctrl:1
	v_cndmask_b32_e64 v85, v95, v103, s[4:5]
	s_nop 1
	v_add_f32_dpp v85, v85, v86 row_ror:8 row_mask:0xf bank_mask:0xf bound_ctrl:1
	v_cndmask_b32_e64 v86, v96, v65, s[4:5]
	v_cndmask_b32_e64 v65, v65, v96, s[4:5]
	s_nop 1
	v_add_f32_dpp v65, v86, v65 row_ror:8 row_mask:0xf bank_mask:0xf bound_ctrl:1
	v_cndmask_b32_e64 v86, v97, v64, s[4:5]
	v_cndmask_b32_e64 v64, v64, v97, s[4:5]
	s_nop 1
	v_add_f32_dpp v64, v86, v64 row_ror:8 row_mask:0xf bank_mask:0xf bound_ctrl:1
	v_cndmask_b32_e64 v86, v98, 0, s[4:5]
	s_nop 1
	v_add_f32_dpp v86, v86, v87 row_ror:8 row_mask:0xf bank_mask:0xf bound_ctrl:1
	v_cndmask_b32_e64 v87, v63, v85, s[6:7]
	v_cndmask_b32_e64 v63, v85, v63, s[6:7]
	v_cndmask_b32_e64 v85, v82, v65, s[6:7]
	v_cndmask_b32_e64 v65, v65, v82, s[6:7]
	v_cndmask_b32_e64 v82, v83, v64, s[6:7]
	v_cndmask_b32_e64 v64, v64, v83, s[6:7]
	v_cndmask_b32_e64 v83, v86, v84, s[6:7]
	v_add_f32_dpp v63, v87, v63 row_half_mirror row_mask:0xf bank_mask:0xf bound_ctrl:1
	v_add_f32_dpp v64, v82, v64 row_half_mirror row_mask:0xf bank_mask:0xf bound_ctrl:1
	v_cndmask_b32_e64 v82, v84, v86, s[6:7]
	v_add_f32_dpp v65, v85, v65 row_half_mirror row_mask:0xf bank_mask:0xf bound_ctrl:1
	s_nop 0
	v_add_f32_dpp v82, v82, v83 row_half_mirror row_mask:0xf bank_mask:0xf bound_ctrl:1
	v_cndmask_b32_e64 v83, v63, v64, s[8:9]
	v_cndmask_b32_e64 v63, v64, v63, s[8:9]
	v_cndmask_b32_e64 v64, v65, v82, s[8:9]
	v_cndmask_b32_e64 v65, v82, v65, s[8:9]
	v_add_f32_dpp v63, v83, v63 quad_perm:[2,3,0,1] row_mask:0xf bank_mask:0xf bound_ctrl:1
	s_nop 0
	v_add_f32_dpp v64, v64, v65 quad_perm:[2,3,0,1] row_mask:0xf bank_mask:0xf bound_ctrl:1
	v_cndmask_b32_e64 v82, v63, v64, s[10:11]
	v_mov_b32_e32 v65, v62
	s_nop 1
	v_mov_b32_dpp v65, v82 quad_perm:[1,0,3,2] row_mask:0xf bank_mask:0xf
	s_and_saveexec_b64 s[0:1], s[14:15]
	s_cbranch_execz .LBB0_73
	v_cndmask_b32_e64 v63, v64, v63, s[10:11]
	v_add_f32_e32 v63, v63, v65
	v_cvt_f16_f32_e32 v63, v63
	v_lshl_add_u32 v64, s34, 5, v117
	ds_write_b16 v64, v63
	s_branch .LBB0_73
